# spatial: the last key block of the max pass stays in registers and is consumed first by the exp/PV pass (one QK recompute fewer)
# speedup vs baseline: 1.0309x; 1.0075x over previous
_Z9k_spatialPKDF16_S0_S0_PfPDF16_:
	s_load_dwordx4 s[4:7], s[0:1], 0x0
	s_load_dwordx2 s[10:11], s[0:1], 0x10
	s_mul_hi_i32 s9, s2, 0x3140
	s_mul_i32 s8, s2, 0x3140
	s_lshl_b64 s[8:9], s[8:9], 1
	v_and_b32_e32 v2, 7, v0
	v_lshrrev_b32_e32 v3, 3, v0
	v_lshlrev_b32_e32 v10, 4, v2
	v_lshl_or_b32 v4, v3, 7, v10
	v_add_u32_e32 v5, 0x1c00, v4
	v_add_u32_e32 v6, 0x3800, v4
	v_add_u32_e32 v7, 0x5400, v4
	v_lshrrev_b32_e32 v8, 1, v0
	v_and_b32_e32 v108, 31, v0
	v_and_b32_e32 v115, 0xe0, v8
	v_or_b32_e32 v109, v115, v108
	s_movk_i32 s3, 0xc5
	v_mov_b32_e32 v8, 0xc4
	v_cmp_gt_u32_e64 s[12:13], s3, v109
	v_bfe_u32 v1, v0, 5, 1
	v_lshlrev_b32_e32 v111, 4, v1
	s_nop 1
	v_cndmask_b32_e64 v110, v8, v109, s[12:13]
	v_lshl_or_b32 v9, v110, 7, v111
	s_movk_i32 s3, 0xe8
	v_cmp_gt_u32_e32 vcc, s3, v0
	v_or_b32_e32 v14, 0x6200, v10
	s_nop 1
	v_cndmask_b32_e32 v7, v14, v7, vcc
	s_waitcnt lgkmcnt(0)
	s_add_u32 s6, s6, s8
	s_addc_u32 s7, s7, s9
	s_add_u32 s10, s10, s8
	s_addc_u32 s11, s11, s9
	s_add_u32 s4, s4, s8
	s_addc_u32 s5, s5, s9
	global_load_dwordx4 v[18:21], v4, s[6:7] nt
	global_load_dwordx4 v[22:25], v4, s[10:11] nt
	global_load_dwordx4 v[26:29], v5, s[6:7] nt
	global_load_dwordx4 v[30:33], v5, s[10:11] nt
	global_load_dwordx4 v[34:37], v6, s[6:7] nt
	global_load_dwordx4 v[38:41], v6, s[10:11] nt
	global_load_dwordx4 v[42:45], v7, s[6:7] nt
	global_load_dwordx4 v[46:49], v7, s[10:11] nt
	global_load_dwordx4 v[74:77], v9, s[4:5] offset:0 nt
	global_load_dwordx4 v[78:81], v9, s[4:5] offset:32 nt
	global_load_dwordx4 v[82:85], v9, s[4:5] offset:64 nt
	global_load_dwordx4 v[86:89], v9, s[4:5] offset:96 nt
	s_movk_i32 s3, 0x90
	v_lshlrev_b32_e32 v11, 3, v2
	v_mul_u32_u24_e32 v16, 0x1c8, v11
	v_mad_u32_u24 v12, v3, s3, v10
	v_lshl_add_u32 v13, v3, 1, v16
	v_mad_u32_u24 v112, v108, s3, v111
	s_waitcnt vmcnt(11)
	ds_write_b128 v12, v[18:21] offset:0
	s_waitcnt vmcnt(10)
	ds_write_b16 v13, v22 offset:32256
	ds_write_b16_d16_hi v13, v22 offset:32712
	ds_write_b16 v13, v23 offset:33168
	ds_write_b16_d16_hi v13, v23 offset:33624
	ds_write_b16 v13, v24 offset:34080
	ds_write_b16_d16_hi v13, v24 offset:34536
	ds_write_b16 v13, v25 offset:34992
	ds_write_b16_d16_hi v13, v25 offset:35448
	s_waitcnt vmcnt(9)
	ds_write_b128 v12, v[26:29] offset:8064
	s_waitcnt vmcnt(8)
	ds_write_b16 v13, v30 offset:32368
	ds_write_b16_d16_hi v13, v30 offset:32824
	ds_write_b16 v13, v31 offset:33280
	ds_write_b16_d16_hi v13, v31 offset:33736
	ds_write_b16 v13, v32 offset:34192
	ds_write_b16_d16_hi v13, v32 offset:34648
	ds_write_b16 v13, v33 offset:35104
	ds_write_b16_d16_hi v13, v33 offset:35560
	s_waitcnt vmcnt(7)
	ds_write_b128 v12, v[34:37] offset:16128
	s_waitcnt vmcnt(6)
	ds_write_b16 v13, v38 offset:32480
	ds_write_b16_d16_hi v13, v38 offset:32936
	ds_write_b16 v13, v39 offset:33392
	ds_write_b16_d16_hi v13, v39 offset:33848
	ds_write_b16 v13, v40 offset:34304
	ds_write_b16_d16_hi v13, v40 offset:34760
	ds_write_b16 v13, v41 offset:35216
	ds_write_b16_d16_hi v13, v41 offset:35672
	s_waitcnt vmcnt(5)
	v_cndmask_b32_e32 v42, 0, v42, vcc
	v_cndmask_b32_e32 v43, 0, v43, vcc
	v_cndmask_b32_e32 v44, 0, v44, vcc
	v_cndmask_b32_e32 v45, 0, v45, vcc
	ds_write_b128 v12, v[42:45] offset:24192
	s_waitcnt vmcnt(4)
	v_cndmask_b32_e32 v46, 0, v46, vcc
	v_cndmask_b32_e32 v47, 0, v47, vcc
	v_cndmask_b32_e32 v48, 0, v48, vcc
	v_cndmask_b32_e32 v49, 0, v49, vcc
	ds_write_b16 v13, v46 offset:32592
	ds_write_b16_d16_hi v13, v46 offset:33048
	ds_write_b16 v13, v47 offset:33504
	ds_write_b16_d16_hi v13, v47 offset:33960
	ds_write_b16 v13, v48 offset:34416
	ds_write_b16_d16_hi v13, v48 offset:34872
	ds_write_b16 v13, v49 offset:35328
	ds_write_b16_d16_hi v13, v49 offset:35784
	s_load_dwordx2 s[8:9], s[0:1], 0x20
	s_load_dwordx2 s[10:11], s[0:1], 0x18
	s_mov_b32 s16, 0x3e38aa3b
	s_mov_b32 s17, 0xf149f2ca
	v_cmp_eq_u32_e64 s[14:15], 0, v1
	v_mul_u32_u24_e32 v113, 0x1c8, v108
	v_lshl_add_u32 v113, v1, 3, v113
	v_add_u32_e32 v113, 0x7e00, v113
	v_add_u32_e32 v114, 0x3900, v113
	v_mov_b32_e32 v106, s17
	s_waitcnt vmcnt(0) lgkmcnt(0)
	s_barrier
	ds_read_b128 v[66:69], v112 offset:0
	ds_read_b128 v[70:73], v112 offset:32
	s_waitcnt lgkmcnt(1)
	v_mfma_f32_32x32x16_f16 v[90:105], v[66:69], v[74:77], 0
	ds_read_b128 v[66:69], v112 offset:64
	s_waitcnt lgkmcnt(1)
	v_mfma_f32_32x32x16_f16 v[90:105], v[70:73], v[78:81], v[90:105]
	ds_read_b128 v[70:73], v112 offset:96
	s_waitcnt lgkmcnt(1)
	v_mfma_f32_32x32x16_f16 v[90:105], v[66:69], v[82:85], v[90:105]
	s_waitcnt lgkmcnt(0)
	v_mfma_f32_32x32x16_f16 v[90:105], v[70:73], v[86:89], v[90:105]
	ds_read_b128 v[66:69], v112 offset:4608
	ds_read_b128 v[70:73], v112 offset:4640
	s_waitcnt lgkmcnt(1)
	v_mfma_f32_32x32x16_f16 v[2:17], v[66:69], v[74:77], 0
	ds_read_b128 v[66:69], v112 offset:4672
	s_waitcnt lgkmcnt(1)
	v_mfma_f32_32x32x16_f16 v[2:17], v[70:73], v[78:81], v[2:17]
	ds_read_b128 v[70:73], v112 offset:4704
	s_waitcnt lgkmcnt(1)
	v_mfma_f32_32x32x16_f16 v[2:17], v[66:69], v[82:85], v[2:17]
	s_waitcnt lgkmcnt(0)
	v_mfma_f32_32x32x16_f16 v[2:17], v[70:73], v[86:89], v[2:17]
	v_max3_f32 v106, v106, v90, v91
	v_max3_f32 v106, v106, v92, v93
	v_max3_f32 v106, v106, v94, v95
	v_max3_f32 v106, v106, v96, v97
	v_max3_f32 v106, v106, v98, v99
	v_max3_f32 v106, v106, v100, v101
	v_max3_f32 v106, v106, v102, v103
	v_max3_f32 v106, v106, v104, v105
	ds_read_b128 v[66:69], v112 offset:9216
	ds_read_b128 v[70:73], v112 offset:9248
	s_waitcnt lgkmcnt(1)
	v_mfma_f32_32x32x16_f16 v[90:105], v[66:69], v[74:77], 0
	ds_read_b128 v[66:69], v112 offset:9280
	s_waitcnt lgkmcnt(1)
	v_mfma_f32_32x32x16_f16 v[90:105], v[70:73], v[78:81], v[90:105]
	ds_read_b128 v[70:73], v112 offset:9312
	s_waitcnt lgkmcnt(1)
	v_mfma_f32_32x32x16_f16 v[90:105], v[66:69], v[82:85], v[90:105]
	s_waitcnt lgkmcnt(0)
	v_mfma_f32_32x32x16_f16 v[90:105], v[70:73], v[86:89], v[90:105]
	v_max3_f32 v106, v106, v2, v3
	v_max3_f32 v106, v106, v4, v5
	v_max3_f32 v106, v106, v6, v7
	v_max3_f32 v106, v106, v8, v9
	v_max3_f32 v106, v106, v10, v11
	v_max3_f32 v106, v106, v12, v13
	v_max3_f32 v106, v106, v14, v15
	v_max3_f32 v106, v106, v16, v17
	ds_read_b128 v[66:69], v112 offset:13824
	ds_read_b128 v[70:73], v112 offset:13856
	s_waitcnt lgkmcnt(1)
	v_mfma_f32_32x32x16_f16 v[2:17], v[66:69], v[74:77], 0
	ds_read_b128 v[66:69], v112 offset:13888
	s_waitcnt lgkmcnt(1)
	v_mfma_f32_32x32x16_f16 v[2:17], v[70:73], v[78:81], v[2:17]
	ds_read_b128 v[70:73], v112 offset:13920
	s_waitcnt lgkmcnt(1)
	v_mfma_f32_32x32x16_f16 v[2:17], v[66:69], v[82:85], v[2:17]
	s_waitcnt lgkmcnt(0)
	v_mfma_f32_32x32x16_f16 v[2:17], v[70:73], v[86:89], v[2:17]
	v_max3_f32 v106, v106, v90, v91
	v_max3_f32 v106, v106, v92, v93
	v_max3_f32 v106, v106, v94, v95
	v_max3_f32 v106, v106, v96, v97
	v_max3_f32 v106, v106, v98, v99
	v_max3_f32 v106, v106, v100, v101
	v_max3_f32 v106, v106, v102, v103
	v_max3_f32 v106, v106, v104, v105
	ds_read_b128 v[66:69], v112 offset:18432
	ds_read_b128 v[70:73], v112 offset:18464
	s_waitcnt lgkmcnt(1)
	v_mfma_f32_32x32x16_f16 v[90:105], v[66:69], v[74:77], 0
	ds_read_b128 v[66:69], v112 offset:18496
	s_waitcnt lgkmcnt(1)
	v_mfma_f32_32x32x16_f16 v[90:105], v[70:73], v[78:81], v[90:105]
	ds_read_b128 v[70:73], v112 offset:18528
	s_waitcnt lgkmcnt(1)
	v_mfma_f32_32x32x16_f16 v[90:105], v[66:69], v[82:85], v[90:105]
	s_waitcnt lgkmcnt(0)
	v_mfma_f32_32x32x16_f16 v[90:105], v[70:73], v[86:89], v[90:105]
	v_max3_f32 v106, v106, v2, v3
	v_max3_f32 v106, v106, v4, v5
	v_max3_f32 v106, v106, v6, v7
	v_max3_f32 v106, v106, v8, v9
	v_max3_f32 v106, v106, v10, v11
	v_max3_f32 v106, v106, v12, v13
	v_max3_f32 v106, v106, v14, v15
	v_max3_f32 v106, v106, v16, v17
	ds_read_b128 v[66:69], v112 offset:23040
	ds_read_b128 v[70:73], v112 offset:23072
	s_waitcnt lgkmcnt(1)
	v_mfma_f32_32x32x16_f16 v[2:17], v[66:69], v[74:77], 0
	ds_read_b128 v[66:69], v112 offset:23104
	s_waitcnt lgkmcnt(1)
	v_mfma_f32_32x32x16_f16 v[2:17], v[70:73], v[78:81], v[2:17]
	ds_read_b128 v[70:73], v112 offset:23136
	s_waitcnt lgkmcnt(1)
	v_mfma_f32_32x32x16_f16 v[2:17], v[66:69], v[82:85], v[2:17]
	s_waitcnt lgkmcnt(0)
	v_mfma_f32_32x32x16_f16 v[2:17], v[70:73], v[86:89], v[2:17]
	v_max3_f32 v106, v106, v90, v91
	v_max3_f32 v106, v106, v92, v93
	v_max3_f32 v106, v106, v94, v95
	v_max3_f32 v106, v106, v96, v97
	v_max3_f32 v106, v106, v98, v99
	v_max3_f32 v106, v106, v100, v101
	v_max3_f32 v106, v106, v102, v103
	v_max3_f32 v106, v106, v104, v105
	ds_read_b128 v[66:69], v112 offset:27648
	ds_read_b128 v[70:73], v112 offset:27680
	s_waitcnt lgkmcnt(1)
	v_mfma_f32_32x32x16_f16 v[90:105], v[66:69], v[74:77], 0
	ds_read_b128 v[66:69], v112 offset:27712
	s_waitcnt lgkmcnt(1)
	v_mfma_f32_32x32x16_f16 v[90:105], v[70:73], v[78:81], v[90:105]
	ds_read_b128 v[70:73], v112 offset:27744
	s_waitcnt lgkmcnt(1)
	v_mfma_f32_32x32x16_f16 v[90:105], v[66:69], v[82:85], v[90:105]
	s_waitcnt lgkmcnt(0)
	v_mfma_f32_32x32x16_f16 v[90:105], v[70:73], v[86:89], v[90:105]
	v_max3_f32 v106, v106, v2, v3
	v_max3_f32 v106, v106, v4, v5
	v_max3_f32 v106, v106, v6, v7
	v_max3_f32 v106, v106, v8, v9
	v_max3_f32 v106, v106, v10, v11
	v_max3_f32 v106, v106, v12, v13
	v_max3_f32 v106, v106, v14, v15
	v_max3_f32 v106, v106, v16, v17
	s_nop 15
	s_nop 1
	v_mov_b32_e32 v94, s17
	v_mov_b32_e32 v95, s17
	v_mov_b32_e32 v96, s17
	v_mov_b32_e32 v97, s17
	v_mov_b32_e32 v98, s17
	v_mov_b32_e32 v99, s17
	v_mov_b32_e32 v100, s17
	v_mov_b32_e32 v101, s17
	v_mov_b32_e32 v102, s17
	v_mov_b32_e32 v103, s17
	v_mov_b32_e32 v104, s17
	v_mov_b32_e32 v105, s17
	v_mov_b32_e32 v120, s17
	v_cndmask_b32_e64 v91, v120, v91, s[14:15]
	v_cndmask_b32_e64 v92, v120, v92, s[14:15]
	v_cndmask_b32_e64 v93, v120, v93, s[14:15]
	v_max3_f32 v106, v106, v90, v91
	v_max3_f32 v106, v106, v92, v93
	v_max3_f32 v106, v106, v94, v95
	v_max3_f32 v106, v106, v96, v97
	v_max3_f32 v106, v106, v98, v99
	v_max3_f32 v106, v106, v100, v101
	v_max3_f32 v106, v106, v102, v103
	v_max3_f32 v106, v106, v104, v105
	v_mov_b32_e32 v120, v106
	v_mov_b32_e32 v121, v106
	s_nop 1
	v_permlane32_swap_b32_e32 v120, v121
	s_nop 1
	v_max3_f32 v106, v106, v120, v121
	v_mul_f32_e32 v106, s16, v106
	v_mov_b32_e32 v107, 0
	v_mov_b32_e32 v18, 0
	v_mov_b32_e32 v19, 0
	v_mov_b32_e32 v20, 0
	v_mov_b32_e32 v21, 0
	v_mov_b32_e32 v22, 0
	v_mov_b32_e32 v23, 0
	v_mov_b32_e32 v24, 0
	v_mov_b32_e32 v25, 0
	v_mov_b32_e32 v26, 0
	v_mov_b32_e32 v27, 0
	v_mov_b32_e32 v28, 0
	v_mov_b32_e32 v29, 0
	v_mov_b32_e32 v30, 0
	v_mov_b32_e32 v31, 0
	v_mov_b32_e32 v32, 0
	v_mov_b32_e32 v33, 0
	v_mov_b32_e32 v34, 0
	v_mov_b32_e32 v35, 0
	v_mov_b32_e32 v36, 0
	v_mov_b32_e32 v37, 0
	v_mov_b32_e32 v38, 0
	v_mov_b32_e32 v39, 0
	v_mov_b32_e32 v40, 0
	v_mov_b32_e32 v41, 0
	v_mov_b32_e32 v42, 0
	v_mov_b32_e32 v43, 0
	v_mov_b32_e32 v44, 0
	v_mov_b32_e32 v45, 0
	v_mov_b32_e32 v46, 0
	v_mov_b32_e32 v47, 0
	v_mov_b32_e32 v48, 0
	v_mov_b32_e32 v49, 0
	ds_read_b128 v[66:69], v112 offset:0
	ds_read_b128 v[70:73], v112 offset:32
	s_waitcnt lgkmcnt(1)
	v_mfma_f32_32x32x16_f16 v[2:17], v[66:69], v[74:77], 0
	ds_read_b128 v[66:69], v112 offset:64
	s_waitcnt lgkmcnt(1)
	v_mfma_f32_32x32x16_f16 v[2:17], v[70:73], v[78:81], v[2:17]
	ds_read_b128 v[70:73], v112 offset:96
	s_waitcnt lgkmcnt(1)
	v_mfma_f32_32x32x16_f16 v[2:17], v[66:69], v[82:85], v[2:17]
	s_waitcnt lgkmcnt(0)
	v_mfma_f32_32x32x16_f16 v[2:17], v[70:73], v[86:89], v[2:17]
	v_fma_f32 v120, v90, s16, -v106
	v_exp_f32_e32 v90, v120
	v_fma_f32 v121, v91, s16, -v106
	v_exp_f32_e32 v91, v121
	v_fma_f32 v122, v92, s16, -v106
	v_exp_f32_e32 v92, v122
	v_fma_f32 v123, v93, s16, -v106
	v_exp_f32_e32 v93, v123
	v_fma_f32 v120, v94, s16, -v106
	v_exp_f32_e32 v94, v120
	v_fma_f32 v121, v95, s16, -v106
	v_exp_f32_e32 v95, v121
	v_fma_f32 v122, v96, s16, -v106
	v_exp_f32_e32 v96, v122
	v_fma_f32 v123, v97, s16, -v106
	v_exp_f32_e32 v97, v123
	v_fma_f32 v120, v98, s16, -v106
	v_exp_f32_e32 v98, v120
	v_fma_f32 v121, v99, s16, -v106
	v_exp_f32_e32 v99, v121
	v_fma_f32 v122, v100, s16, -v106
	v_exp_f32_e32 v100, v122
	v_fma_f32 v123, v101, s16, -v106
	v_exp_f32_e32 v101, v123
	v_fma_f32 v120, v102, s16, -v106
	v_exp_f32_e32 v102, v120
	v_fma_f32 v121, v103, s16, -v106
	v_exp_f32_e32 v103, v121
	v_fma_f32 v122, v104, s16, -v106
	v_exp_f32_e32 v104, v122
	v_fma_f32 v123, v105, s16, -v106
	v_exp_f32_e32 v105, v123
	v_add_f32_e32 v107, v107, v90
	v_add_f32_e32 v107, v107, v91
	v_add_f32_e32 v107, v107, v92
	v_add_f32_e32 v107, v107, v93
	v_add_f32_e32 v107, v107, v94
	v_add_f32_e32 v107, v107, v95
	v_add_f32_e32 v107, v107, v96
	v_add_f32_e32 v107, v107, v97
	v_add_f32_e32 v107, v107, v98
	v_add_f32_e32 v107, v107, v99
	v_add_f32_e32 v107, v107, v100
	v_add_f32_e32 v107, v107, v101
	v_add_f32_e32 v107, v107, v102
	v_add_f32_e32 v107, v107, v103
	v_add_f32_e32 v107, v107, v104
	v_add_f32_e32 v107, v107, v105
	ds_read2_b64 v[58:61], v113 offset0:48 offset1:50
	ds_read2_b64 v[62:65], v114 offset0:48 offset1:50
	v_cvt_pk_f16_f32 v50, v90, v91
	v_cvt_pk_f16_f32 v51, v92, v93
	v_cvt_pk_f16_f32 v52, v94, v95
	v_cvt_pk_f16_f32 v53, v96, v97
	v_cvt_pk_f16_f32 v54, v98, v99
	v_cvt_pk_f16_f32 v55, v100, v101
	v_cvt_pk_f16_f32 v56, v102, v103
	v_cvt_pk_f16_f32 v57, v104, v105
	s_nop 1
	s_waitcnt lgkmcnt(1)
	v_mfma_f32_32x32x16_f16 v[18:33], v[58:61], v[50:53], v[18:33]
	ds_read2_b64 v[58:61], v113 offset0:52 offset1:54
	s_waitcnt lgkmcnt(1)
	v_mfma_f32_32x32x16_f16 v[34:49], v[62:65], v[50:53], v[34:49]
	ds_read2_b64 v[62:65], v114 offset0:52 offset1:54
	s_waitcnt lgkmcnt(1)
	v_mfma_f32_32x32x16_f16 v[18:33], v[58:61], v[54:57], v[18:33]
	s_waitcnt lgkmcnt(0)
	v_mfma_f32_32x32x16_f16 v[34:49], v[62:65], v[54:57], v[34:49]
	ds_read_b128 v[66:69], v112 offset:4608
	ds_read_b128 v[70:73], v112 offset:4640
	s_waitcnt lgkmcnt(1)
	v_mfma_f32_32x32x16_f16 v[90:105], v[66:69], v[74:77], 0
	ds_read_b128 v[66:69], v112 offset:4672
	s_waitcnt lgkmcnt(1)
	v_mfma_f32_32x32x16_f16 v[90:105], v[70:73], v[78:81], v[90:105]
	ds_read_b128 v[70:73], v112 offset:4704
	s_waitcnt lgkmcnt(1)
	v_mfma_f32_32x32x16_f16 v[90:105], v[66:69], v[82:85], v[90:105]
	s_waitcnt lgkmcnt(0)
	v_mfma_f32_32x32x16_f16 v[90:105], v[70:73], v[86:89], v[90:105]
	v_fma_f32 v120, v2, s16, -v106
	v_exp_f32_e32 v2, v120
	v_fma_f32 v121, v3, s16, -v106
	v_exp_f32_e32 v3, v121
	v_fma_f32 v122, v4, s16, -v106
	v_exp_f32_e32 v4, v122
	v_fma_f32 v123, v5, s16, -v106
	v_exp_f32_e32 v5, v123
	v_fma_f32 v120, v6, s16, -v106
	v_exp_f32_e32 v6, v120
	v_fma_f32 v121, v7, s16, -v106
	v_exp_f32_e32 v7, v121
	v_fma_f32 v122, v8, s16, -v106
	v_exp_f32_e32 v8, v122
	v_fma_f32 v123, v9, s16, -v106
	v_exp_f32_e32 v9, v123
	v_fma_f32 v120, v10, s16, -v106
	v_exp_f32_e32 v10, v120
	v_fma_f32 v121, v11, s16, -v106
	v_exp_f32_e32 v11, v121
	v_fma_f32 v122, v12, s16, -v106
	v_exp_f32_e32 v12, v122
	v_fma_f32 v123, v13, s16, -v106
	v_exp_f32_e32 v13, v123
	v_fma_f32 v120, v14, s16, -v106
	v_exp_f32_e32 v14, v120
	v_fma_f32 v121, v15, s16, -v106
	v_exp_f32_e32 v15, v121
	v_fma_f32 v122, v16, s16, -v106
	v_exp_f32_e32 v16, v122
	v_fma_f32 v123, v17, s16, -v106
	v_exp_f32_e32 v17, v123
	v_add_f32_e32 v107, v107, v2
	v_add_f32_e32 v107, v107, v3
	v_add_f32_e32 v107, v107, v4
	v_add_f32_e32 v107, v107, v5
	v_add_f32_e32 v107, v107, v6
	v_add_f32_e32 v107, v107, v7
	v_add_f32_e32 v107, v107, v8
	v_add_f32_e32 v107, v107, v9
	v_add_f32_e32 v107, v107, v10
	v_add_f32_e32 v107, v107, v11
	v_add_f32_e32 v107, v107, v12
	v_add_f32_e32 v107, v107, v13
	v_add_f32_e32 v107, v107, v14
	v_add_f32_e32 v107, v107, v15
	v_add_f32_e32 v107, v107, v16
	v_add_f32_e32 v107, v107, v17
	ds_read2_b64 v[58:61], v113 offset0:0 offset1:2
	ds_read2_b64 v[62:65], v114 offset0:0 offset1:2
	v_cvt_pk_f16_f32 v50, v2, v3
	v_cvt_pk_f16_f32 v51, v4, v5
	v_cvt_pk_f16_f32 v52, v6, v7
	v_cvt_pk_f16_f32 v53, v8, v9
	v_cvt_pk_f16_f32 v54, v10, v11
	v_cvt_pk_f16_f32 v55, v12, v13
	v_cvt_pk_f16_f32 v56, v14, v15
	v_cvt_pk_f16_f32 v57, v16, v17
	s_nop 1
	s_waitcnt lgkmcnt(1)
	v_mfma_f32_32x32x16_f16 v[18:33], v[58:61], v[50:53], v[18:33]
	ds_read2_b64 v[58:61], v113 offset0:4 offset1:6
	s_waitcnt lgkmcnt(1)
	v_mfma_f32_32x32x16_f16 v[34:49], v[62:65], v[50:53], v[34:49]
	ds_read2_b64 v[62:65], v114 offset0:4 offset1:6
	s_waitcnt lgkmcnt(1)
	v_mfma_f32_32x32x16_f16 v[18:33], v[58:61], v[54:57], v[18:33]
	s_waitcnt lgkmcnt(0)
	v_mfma_f32_32x32x16_f16 v[34:49], v[62:65], v[54:57], v[34:49]
	ds_read_b128 v[66:69], v112 offset:9216
	ds_read_b128 v[70:73], v112 offset:9248
	s_waitcnt lgkmcnt(1)
	v_mfma_f32_32x32x16_f16 v[2:17], v[66:69], v[74:77], 0
	ds_read_b128 v[66:69], v112 offset:9280
	s_waitcnt lgkmcnt(1)
	v_mfma_f32_32x32x16_f16 v[2:17], v[70:73], v[78:81], v[2:17]
	ds_read_b128 v[70:73], v112 offset:9312
	s_waitcnt lgkmcnt(1)
	v_mfma_f32_32x32x16_f16 v[2:17], v[66:69], v[82:85], v[2:17]
	s_waitcnt lgkmcnt(0)
	v_mfma_f32_32x32x16_f16 v[2:17], v[70:73], v[86:89], v[2:17]
	v_fma_f32 v120, v90, s16, -v106
	v_exp_f32_e32 v90, v120
	v_fma_f32 v121, v91, s16, -v106
	v_exp_f32_e32 v91, v121
	v_fma_f32 v122, v92, s16, -v106
	v_exp_f32_e32 v92, v122
	v_fma_f32 v123, v93, s16, -v106
	v_exp_f32_e32 v93, v123
	v_fma_f32 v120, v94, s16, -v106
	v_exp_f32_e32 v94, v120
	v_fma_f32 v121, v95, s16, -v106
	v_exp_f32_e32 v95, v121
	v_fma_f32 v122, v96, s16, -v106
	v_exp_f32_e32 v96, v122
	v_fma_f32 v123, v97, s16, -v106
	v_exp_f32_e32 v97, v123
	v_fma_f32 v120, v98, s16, -v106
	v_exp_f32_e32 v98, v120
	v_fma_f32 v121, v99, s16, -v106
	v_exp_f32_e32 v99, v121
	v_fma_f32 v122, v100, s16, -v106
	v_exp_f32_e32 v100, v122
	v_fma_f32 v123, v101, s16, -v106
	v_exp_f32_e32 v101, v123
	v_fma_f32 v120, v102, s16, -v106
	v_exp_f32_e32 v102, v120
	v_fma_f32 v121, v103, s16, -v106
	v_exp_f32_e32 v103, v121
	v_fma_f32 v122, v104, s16, -v106
	v_exp_f32_e32 v104, v122
	v_fma_f32 v123, v105, s16, -v106
	v_exp_f32_e32 v105, v123
	v_add_f32_e32 v107, v107, v90
	v_add_f32_e32 v107, v107, v91
	v_add_f32_e32 v107, v107, v92
	v_add_f32_e32 v107, v107, v93
	v_add_f32_e32 v107, v107, v94
	v_add_f32_e32 v107, v107, v95
	v_add_f32_e32 v107, v107, v96
	v_add_f32_e32 v107, v107, v97
	v_add_f32_e32 v107, v107, v98
	v_add_f32_e32 v107, v107, v99
	v_add_f32_e32 v107, v107, v100
	v_add_f32_e32 v107, v107, v101
	v_add_f32_e32 v107, v107, v102
	v_add_f32_e32 v107, v107, v103
	v_add_f32_e32 v107, v107, v104
	v_add_f32_e32 v107, v107, v105
	ds_read2_b64 v[58:61], v113 offset0:8 offset1:10
	ds_read2_b64 v[62:65], v114 offset0:8 offset1:10
	v_cvt_pk_f16_f32 v50, v90, v91
	v_cvt_pk_f16_f32 v51, v92, v93
	v_cvt_pk_f16_f32 v52, v94, v95
	v_cvt_pk_f16_f32 v53, v96, v97
	v_cvt_pk_f16_f32 v54, v98, v99
	v_cvt_pk_f16_f32 v55, v100, v101
	v_cvt_pk_f16_f32 v56, v102, v103
	v_cvt_pk_f16_f32 v57, v104, v105
	s_nop 1
	s_waitcnt lgkmcnt(1)
	v_mfma_f32_32x32x16_f16 v[18:33], v[58:61], v[50:53], v[18:33]
	ds_read2_b64 v[58:61], v113 offset0:12 offset1:14
	s_waitcnt lgkmcnt(1)
	v_mfma_f32_32x32x16_f16 v[34:49], v[62:65], v[50:53], v[34:49]
	ds_read2_b64 v[62:65], v114 offset0:12 offset1:14
	s_waitcnt lgkmcnt(1)
	v_mfma_f32_32x32x16_f16 v[18:33], v[58:61], v[54:57], v[18:33]
	s_waitcnt lgkmcnt(0)
	v_mfma_f32_32x32x16_f16 v[34:49], v[62:65], v[54:57], v[34:49]
	ds_read_b128 v[66:69], v112 offset:13824
	ds_read_b128 v[70:73], v112 offset:13856
	s_waitcnt lgkmcnt(1)
	v_mfma_f32_32x32x16_f16 v[90:105], v[66:69], v[74:77], 0
	ds_read_b128 v[66:69], v112 offset:13888
	s_waitcnt lgkmcnt(1)
	v_mfma_f32_32x32x16_f16 v[90:105], v[70:73], v[78:81], v[90:105]
	ds_read_b128 v[70:73], v112 offset:13920
	s_waitcnt lgkmcnt(1)
	v_mfma_f32_32x32x16_f16 v[90:105], v[66:69], v[82:85], v[90:105]
	s_waitcnt lgkmcnt(0)
	v_mfma_f32_32x32x16_f16 v[90:105], v[70:73], v[86:89], v[90:105]
	v_fma_f32 v120, v2, s16, -v106
	v_exp_f32_e32 v2, v120
	v_fma_f32 v121, v3, s16, -v106
	v_exp_f32_e32 v3, v121
	v_fma_f32 v122, v4, s16, -v106
	v_exp_f32_e32 v4, v122
	v_fma_f32 v123, v5, s16, -v106
	v_exp_f32_e32 v5, v123
	v_fma_f32 v120, v6, s16, -v106
	v_exp_f32_e32 v6, v120
	v_fma_f32 v121, v7, s16, -v106
	v_exp_f32_e32 v7, v121
	v_fma_f32 v122, v8, s16, -v106
	v_exp_f32_e32 v8, v122
	v_fma_f32 v123, v9, s16, -v106
	v_exp_f32_e32 v9, v123
	v_fma_f32 v120, v10, s16, -v106
	v_exp_f32_e32 v10, v120
	v_fma_f32 v121, v11, s16, -v106
	v_exp_f32_e32 v11, v121
	v_fma_f32 v122, v12, s16, -v106
	v_exp_f32_e32 v12, v122
	v_fma_f32 v123, v13, s16, -v106
	v_exp_f32_e32 v13, v123
	v_fma_f32 v120, v14, s16, -v106
	v_exp_f32_e32 v14, v120
	v_fma_f32 v121, v15, s16, -v106
	v_exp_f32_e32 v15, v121
	v_fma_f32 v122, v16, s16, -v106
	v_exp_f32_e32 v16, v122
	v_fma_f32 v123, v17, s16, -v106
	v_exp_f32_e32 v17, v123
	v_add_f32_e32 v107, v107, v2
	v_add_f32_e32 v107, v107, v3
	v_add_f32_e32 v107, v107, v4
	v_add_f32_e32 v107, v107, v5
	v_add_f32_e32 v107, v107, v6
	v_add_f32_e32 v107, v107, v7
	v_add_f32_e32 v107, v107, v8
	v_add_f32_e32 v107, v107, v9
	v_add_f32_e32 v107, v107, v10
	v_add_f32_e32 v107, v107, v11
	v_add_f32_e32 v107, v107, v12
	v_add_f32_e32 v107, v107, v13
	v_add_f32_e32 v107, v107, v14
	v_add_f32_e32 v107, v107, v15
	v_add_f32_e32 v107, v107, v16
	v_add_f32_e32 v107, v107, v17
	ds_read2_b64 v[58:61], v113 offset0:16 offset1:18
	ds_read2_b64 v[62:65], v114 offset0:16 offset1:18
	v_cvt_pk_f16_f32 v50, v2, v3
	v_cvt_pk_f16_f32 v51, v4, v5
	v_cvt_pk_f16_f32 v52, v6, v7
	v_cvt_pk_f16_f32 v53, v8, v9
	v_cvt_pk_f16_f32 v54, v10, v11
	v_cvt_pk_f16_f32 v55, v12, v13
	v_cvt_pk_f16_f32 v56, v14, v15
	v_cvt_pk_f16_f32 v57, v16, v17
	s_nop 1
	s_waitcnt lgkmcnt(1)
	v_mfma_f32_32x32x16_f16 v[18:33], v[58:61], v[50:53], v[18:33]
	ds_read2_b64 v[58:61], v113 offset0:20 offset1:22
	s_waitcnt lgkmcnt(1)
	v_mfma_f32_32x32x16_f16 v[34:49], v[62:65], v[50:53], v[34:49]
	ds_read2_b64 v[62:65], v114 offset0:20 offset1:22
	s_waitcnt lgkmcnt(1)
	v_mfma_f32_32x32x16_f16 v[18:33], v[58:61], v[54:57], v[18:33]
	s_waitcnt lgkmcnt(0)
	v_mfma_f32_32x32x16_f16 v[34:49], v[62:65], v[54:57], v[34:49]
	ds_read_b128 v[66:69], v112 offset:18432
	ds_read_b128 v[70:73], v112 offset:18464
	s_waitcnt lgkmcnt(1)
	v_mfma_f32_32x32x16_f16 v[2:17], v[66:69], v[74:77], 0
	ds_read_b128 v[66:69], v112 offset:18496
	s_waitcnt lgkmcnt(1)
	v_mfma_f32_32x32x16_f16 v[2:17], v[70:73], v[78:81], v[2:17]
	ds_read_b128 v[70:73], v112 offset:18528
	s_waitcnt lgkmcnt(1)
	v_mfma_f32_32x32x16_f16 v[2:17], v[66:69], v[82:85], v[2:17]
	s_waitcnt lgkmcnt(0)
	v_mfma_f32_32x32x16_f16 v[2:17], v[70:73], v[86:89], v[2:17]
	v_fma_f32 v120, v90, s16, -v106
	v_exp_f32_e32 v90, v120
	v_fma_f32 v121, v91, s16, -v106
	v_exp_f32_e32 v91, v121
	v_fma_f32 v122, v92, s16, -v106
	v_exp_f32_e32 v92, v122
	v_fma_f32 v123, v93, s16, -v106
	v_exp_f32_e32 v93, v123
	v_fma_f32 v120, v94, s16, -v106
	v_exp_f32_e32 v94, v120
	v_fma_f32 v121, v95, s16, -v106
	v_exp_f32_e32 v95, v121
	v_fma_f32 v122, v96, s16, -v106
	v_exp_f32_e32 v96, v122
	v_fma_f32 v123, v97, s16, -v106
	v_exp_f32_e32 v97, v123
	v_fma_f32 v120, v98, s16, -v106
	v_exp_f32_e32 v98, v120
	v_fma_f32 v121, v99, s16, -v106
	v_exp_f32_e32 v99, v121
	v_fma_f32 v122, v100, s16, -v106
	v_exp_f32_e32 v100, v122
	v_fma_f32 v123, v101, s16, -v106
	v_exp_f32_e32 v101, v123
	v_fma_f32 v120, v102, s16, -v106
	v_exp_f32_e32 v102, v120
	v_fma_f32 v121, v103, s16, -v106
	v_exp_f32_e32 v103, v121
	v_fma_f32 v122, v104, s16, -v106
	v_exp_f32_e32 v104, v122
	v_fma_f32 v123, v105, s16, -v106
	v_exp_f32_e32 v105, v123
	v_add_f32_e32 v107, v107, v90
	v_add_f32_e32 v107, v107, v91
	v_add_f32_e32 v107, v107, v92
	v_add_f32_e32 v107, v107, v93
	v_add_f32_e32 v107, v107, v94
	v_add_f32_e32 v107, v107, v95
	v_add_f32_e32 v107, v107, v96
	v_add_f32_e32 v107, v107, v97
	v_add_f32_e32 v107, v107, v98
	v_add_f32_e32 v107, v107, v99
	v_add_f32_e32 v107, v107, v100
	v_add_f32_e32 v107, v107, v101
	v_add_f32_e32 v107, v107, v102
	v_add_f32_e32 v107, v107, v103
	v_add_f32_e32 v107, v107, v104
	v_add_f32_e32 v107, v107, v105
	ds_read2_b64 v[58:61], v113 offset0:24 offset1:26
	ds_read2_b64 v[62:65], v114 offset0:24 offset1:26
	v_cvt_pk_f16_f32 v50, v90, v91
	v_cvt_pk_f16_f32 v51, v92, v93
	v_cvt_pk_f16_f32 v52, v94, v95
	v_cvt_pk_f16_f32 v53, v96, v97
	v_cvt_pk_f16_f32 v54, v98, v99
	v_cvt_pk_f16_f32 v55, v100, v101
	v_cvt_pk_f16_f32 v56, v102, v103
	v_cvt_pk_f16_f32 v57, v104, v105
	s_nop 1
	s_waitcnt lgkmcnt(1)
	v_mfma_f32_32x32x16_f16 v[18:33], v[58:61], v[50:53], v[18:33]
	ds_read2_b64 v[58:61], v113 offset0:28 offset1:30
	s_waitcnt lgkmcnt(1)
	v_mfma_f32_32x32x16_f16 v[34:49], v[62:65], v[50:53], v[34:49]
	ds_read2_b64 v[62:65], v114 offset0:28 offset1:30
	s_waitcnt lgkmcnt(1)
	v_mfma_f32_32x32x16_f16 v[18:33], v[58:61], v[54:57], v[18:33]
	s_waitcnt lgkmcnt(0)
	v_mfma_f32_32x32x16_f16 v[34:49], v[62:65], v[54:57], v[34:49]
	ds_read_b128 v[66:69], v112 offset:23040
	ds_read_b128 v[70:73], v112 offset:23072
	s_waitcnt lgkmcnt(1)
	v_mfma_f32_32x32x16_f16 v[90:105], v[66:69], v[74:77], 0
	ds_read_b128 v[66:69], v112 offset:23104
	s_waitcnt lgkmcnt(1)
	v_mfma_f32_32x32x16_f16 v[90:105], v[70:73], v[78:81], v[90:105]
	ds_read_b128 v[70:73], v112 offset:23136
	s_waitcnt lgkmcnt(1)
	v_mfma_f32_32x32x16_f16 v[90:105], v[66:69], v[82:85], v[90:105]
	s_waitcnt lgkmcnt(0)
	v_mfma_f32_32x32x16_f16 v[90:105], v[70:73], v[86:89], v[90:105]
	v_fma_f32 v120, v2, s16, -v106
	v_exp_f32_e32 v2, v120
	v_fma_f32 v121, v3, s16, -v106
	v_exp_f32_e32 v3, v121
	v_fma_f32 v122, v4, s16, -v106
	v_exp_f32_e32 v4, v122
	v_fma_f32 v123, v5, s16, -v106
	v_exp_f32_e32 v5, v123
	v_fma_f32 v120, v6, s16, -v106
	v_exp_f32_e32 v6, v120
	v_fma_f32 v121, v7, s16, -v106
	v_exp_f32_e32 v7, v121
	v_fma_f32 v122, v8, s16, -v106
	v_exp_f32_e32 v8, v122
	v_fma_f32 v123, v9, s16, -v106
	v_exp_f32_e32 v9, v123
	v_fma_f32 v120, v10, s16, -v106
	v_exp_f32_e32 v10, v120
	v_fma_f32 v121, v11, s16, -v106
	v_exp_f32_e32 v11, v121
	v_fma_f32 v122, v12, s16, -v106
	v_exp_f32_e32 v12, v122
	v_fma_f32 v123, v13, s16, -v106
	v_exp_f32_e32 v13, v123
	v_fma_f32 v120, v14, s16, -v106
	v_exp_f32_e32 v14, v120
	v_fma_f32 v121, v15, s16, -v106
	v_exp_f32_e32 v15, v121
	v_fma_f32 v122, v16, s16, -v106
	v_exp_f32_e32 v16, v122
	v_fma_f32 v123, v17, s16, -v106
	v_exp_f32_e32 v17, v123
	v_add_f32_e32 v107, v107, v2
	v_add_f32_e32 v107, v107, v3
	v_add_f32_e32 v107, v107, v4
	v_add_f32_e32 v107, v107, v5
	v_add_f32_e32 v107, v107, v6
	v_add_f32_e32 v107, v107, v7
	v_add_f32_e32 v107, v107, v8
	v_add_f32_e32 v107, v107, v9
	v_add_f32_e32 v107, v107, v10
	v_add_f32_e32 v107, v107, v11
	v_add_f32_e32 v107, v107, v12
	v_add_f32_e32 v107, v107, v13
	v_add_f32_e32 v107, v107, v14
	v_add_f32_e32 v107, v107, v15
	v_add_f32_e32 v107, v107, v16
	v_add_f32_e32 v107, v107, v17
	ds_read2_b64 v[58:61], v113 offset0:32 offset1:34
	ds_read2_b64 v[62:65], v114 offset0:32 offset1:34
	v_cvt_pk_f16_f32 v50, v2, v3
	v_cvt_pk_f16_f32 v51, v4, v5
	v_cvt_pk_f16_f32 v52, v6, v7
	v_cvt_pk_f16_f32 v53, v8, v9
	v_cvt_pk_f16_f32 v54, v10, v11
	v_cvt_pk_f16_f32 v55, v12, v13
	v_cvt_pk_f16_f32 v56, v14, v15
	v_cvt_pk_f16_f32 v57, v16, v17
	s_nop 1
	s_waitcnt lgkmcnt(1)
	v_mfma_f32_32x32x16_f16 v[18:33], v[58:61], v[50:53], v[18:33]
	ds_read2_b64 v[58:61], v113 offset0:36 offset1:38
	s_waitcnt lgkmcnt(1)
	v_mfma_f32_32x32x16_f16 v[34:49], v[62:65], v[50:53], v[34:49]
	ds_read2_b64 v[62:65], v114 offset0:36 offset1:38
	s_waitcnt lgkmcnt(1)
	v_mfma_f32_32x32x16_f16 v[18:33], v[58:61], v[54:57], v[18:33]
	s_waitcnt lgkmcnt(0)
	v_mfma_f32_32x32x16_f16 v[34:49], v[62:65], v[54:57], v[34:49]
	s_nop 15
	s_nop 1
	v_fma_f32 v120, v90, s16, -v106
	v_exp_f32_e32 v90, v120
	v_fma_f32 v121, v91, s16, -v106
	v_exp_f32_e32 v91, v121
	v_fma_f32 v122, v92, s16, -v106
	v_exp_f32_e32 v92, v122
	v_fma_f32 v123, v93, s16, -v106
	v_exp_f32_e32 v93, v123
	v_fma_f32 v120, v94, s16, -v106
	v_exp_f32_e32 v94, v120
	v_fma_f32 v121, v95, s16, -v106
	v_exp_f32_e32 v95, v121
	v_fma_f32 v122, v96, s16, -v106
	v_exp_f32_e32 v96, v122
	v_fma_f32 v123, v97, s16, -v106
	v_exp_f32_e32 v97, v123
	v_fma_f32 v120, v98, s16, -v106
	v_exp_f32_e32 v98, v120
	v_fma_f32 v121, v99, s16, -v106
	v_exp_f32_e32 v99, v121
	v_fma_f32 v122, v100, s16, -v106
	v_exp_f32_e32 v100, v122
	v_fma_f32 v123, v101, s16, -v106
	v_exp_f32_e32 v101, v123
	v_fma_f32 v120, v102, s16, -v106
	v_exp_f32_e32 v102, v120
	v_fma_f32 v121, v103, s16, -v106
	v_exp_f32_e32 v103, v121
	v_fma_f32 v122, v104, s16, -v106
	v_exp_f32_e32 v104, v122
	v_fma_f32 v123, v105, s16, -v106
	v_exp_f32_e32 v105, v123
	v_add_f32_e32 v107, v107, v90
	v_add_f32_e32 v107, v107, v91
	v_add_f32_e32 v107, v107, v92
	v_add_f32_e32 v107, v107, v93
	v_add_f32_e32 v107, v107, v94
	v_add_f32_e32 v107, v107, v95
	v_add_f32_e32 v107, v107, v96
	v_add_f32_e32 v107, v107, v97
	v_add_f32_e32 v107, v107, v98
	v_add_f32_e32 v107, v107, v99
	v_add_f32_e32 v107, v107, v100
	v_add_f32_e32 v107, v107, v101
	v_add_f32_e32 v107, v107, v102
	v_add_f32_e32 v107, v107, v103
	v_add_f32_e32 v107, v107, v104
	v_add_f32_e32 v107, v107, v105
	ds_read2_b64 v[58:61], v113 offset0:40 offset1:42
	ds_read2_b64 v[62:65], v114 offset0:40 offset1:42
	v_cvt_pk_f16_f32 v50, v90, v91
	v_cvt_pk_f16_f32 v51, v92, v93
	v_cvt_pk_f16_f32 v52, v94, v95
	v_cvt_pk_f16_f32 v53, v96, v97
	v_cvt_pk_f16_f32 v54, v98, v99
	v_cvt_pk_f16_f32 v55, v100, v101
	v_cvt_pk_f16_f32 v56, v102, v103
	v_cvt_pk_f16_f32 v57, v104, v105
	s_nop 1
	s_waitcnt lgkmcnt(1)
	v_mfma_f32_32x32x16_f16 v[18:33], v[58:61], v[50:53], v[18:33]
	ds_read2_b64 v[58:61], v113 offset0:44 offset1:46
	s_waitcnt lgkmcnt(1)
	v_mfma_f32_32x32x16_f16 v[34:49], v[62:65], v[50:53], v[34:49]
	ds_read2_b64 v[62:65], v114 offset0:44 offset1:46
	s_waitcnt lgkmcnt(1)
	v_mfma_f32_32x32x16_f16 v[18:33], v[58:61], v[54:57], v[18:33]
	s_waitcnt lgkmcnt(0)
	v_mfma_f32_32x32x16_f16 v[34:49], v[62:65], v[54:57], v[34:49]
	v_mov_b32_e32 v120, v107
	v_mov_b32_e32 v121, v107
	s_nop 1
	v_permlane32_swap_b32_e32 v120, v121
	s_nop 1
	v_add_f32_e32 v107, v120, v121
	v_log_f32_e32 v122, v107
	v_rcp_f32_e32 v123, v107
	s_nop 0
	v_add_f32_e32 v122, v122, v106
	v_fma_f32 v124, -v107, v123, 2.0
	v_mul_f32_e32 v123, v123, v124
	v_lshlrev_b32_e32 v125, 2, v109
	s_mov_b64 s[18:19], exec
	s_and_b64 exec, exec, s[14:15]
	ds_write_b32 v125, v122 offset:61440
	s_mov_b64 exec, s[18:19]
	s_mul_i32 s20, s2, 0x493
	s_lshr_b32 s20, s20, 16
	s_mul_i32 s21, s20, 56
	s_sub_u32 s21, s2, s21
	s_mul_i32 s22, s21, 0x2493
	s_lshr_b32 s22, s22, 16
	s_mul_i32 s23, s22, 7
	s_sub_u32 s23, s21, s23
	s_mul_i32 s24, s23, 0xc5
	s_lshl_b32 s24, s24, 13
	s_lshl_b32 s25, s22, 10
	s_add_u32 s24, s24, s25
	s_lshl_b32 s25, s20, 7
	s_add_u32 s24, s24, s25
	v_lshlrev_b32_e32 v125, 13, v110
	v_add3_u32 v125, v125, s24, v111
	s_nop 15
	s_waitcnt lgkmcnt(0)
	v_mul_f32_e32 v18, v18, v123
	v_mul_f32_e32 v19, v19, v123
	v_mul_f32_e32 v20, v20, v123
	v_mul_f32_e32 v21, v21, v123
	v_mul_f32_e32 v22, v22, v123
	v_mul_f32_e32 v23, v23, v123
	v_mul_f32_e32 v24, v24, v123
	v_mul_f32_e32 v25, v25, v123
	v_cvt_pk_f16_f32 v50, v18, v19
	v_cvt_pk_f16_f32 v51, v20, v21
	v_cvt_pk_f16_f32 v52, v22, v23
	v_cvt_pk_f16_f32 v53, v24, v25
	s_nop 1
	v_permlane32_swap_b32_e32 v50, v52
	v_permlane32_swap_b32_e32 v51, v53
	s_nop 1
	s_and_b64 exec, exec, s[12:13]
	global_store_dwordx4 v125, v[50:53], s[8:9] offset:0
	s_mov_b64 exec, s[18:19]
	s_nop 1
	v_mul_f32_e32 v26, v26, v123
	v_mul_f32_e32 v27, v27, v123
	v_mul_f32_e32 v28, v28, v123
	v_mul_f32_e32 v29, v29, v123
	v_mul_f32_e32 v30, v30, v123
	v_mul_f32_e32 v31, v31, v123
	v_mul_f32_e32 v32, v32, v123
	v_mul_f32_e32 v33, v33, v123
	v_cvt_pk_f16_f32 v54, v26, v27
	v_cvt_pk_f16_f32 v55, v28, v29
	v_cvt_pk_f16_f32 v56, v30, v31
	v_cvt_pk_f16_f32 v57, v32, v33
	s_nop 1
	v_permlane32_swap_b32_e32 v54, v56
	v_permlane32_swap_b32_e32 v55, v57
	s_nop 1
	s_and_b64 exec, exec, s[12:13]
	global_store_dwordx4 v125, v[54:57], s[8:9] offset:32
	s_mov_b64 exec, s[18:19]
	s_nop 1
	v_mul_f32_e32 v34, v34, v123
	v_mul_f32_e32 v35, v35, v123
	v_mul_f32_e32 v36, v36, v123
	v_mul_f32_e32 v37, v37, v123
	v_mul_f32_e32 v38, v38, v123
	v_mul_f32_e32 v39, v39, v123
	v_mul_f32_e32 v40, v40, v123
	v_mul_f32_e32 v41, v41, v123
	v_cvt_pk_f16_f32 v50, v34, v35
	v_cvt_pk_f16_f32 v51, v36, v37
	v_cvt_pk_f16_f32 v52, v38, v39
	v_cvt_pk_f16_f32 v53, v40, v41
	s_nop 1
	v_permlane32_swap_b32_e32 v50, v52
	v_permlane32_swap_b32_e32 v51, v53
	s_nop 1
	s_and_b64 exec, exec, s[12:13]
	global_store_dwordx4 v125, v[50:53], s[8:9] offset:64
	s_mov_b64 exec, s[18:19]
	s_nop 1
	v_mul_f32_e32 v42, v42, v123
	v_mul_f32_e32 v43, v43, v123
	v_mul_f32_e32 v44, v44, v123
	v_mul_f32_e32 v45, v45, v123
	v_mul_f32_e32 v46, v46, v123
	v_mul_f32_e32 v47, v47, v123
	v_mul_f32_e32 v48, v48, v123
	v_mul_f32_e32 v49, v49, v123
	v_cvt_pk_f16_f32 v54, v42, v43
	v_cvt_pk_f16_f32 v55, v44, v45
	v_cvt_pk_f16_f32 v56, v46, v47
	v_cvt_pk_f16_f32 v57, v48, v49
	s_nop 1
	v_permlane32_swap_b32_e32 v54, v56
	v_permlane32_swap_b32_e32 v55, v57
	s_nop 1
	s_and_b64 exec, exec, s[12:13]
	global_store_dwordx4 v125, v[54:57], s[8:9] offset:96
	s_mov_b64 exec, s[18:19]
	s_nop 1
	s_waitcnt lgkmcnt(0)
	s_barrier
	v_lshl_add_u32 v120, v115, 2, v111
	ds_read_b128 v[90:93], v120 offset:61440
	ds_read_b128 v[94:97], v120 offset:61472
	ds_read_b128 v[98:101], v120 offset:61504
	ds_read_b128 v[102:105], v120 offset:61536
	v_lshl_or_b32 v121, v1, 2, v115
	v_mul_u32_u24_e32 v121, 0xc5, v121
	v_add_lshl_u32 v116, v121, v108, 2
	v_add_u32_e32 v117, 0x18a0, v116
	v_add_u32_e32 v118, 0x3140, v116
	v_add_u32_e32 v119, 0x49e0, v116
	s_mul_hi_u32 s21, s2, 0x25e64
	s_mul_i32 s20, s2, 0x25e64
	s_add_u32 s10, s10, s20
	s_addc_u32 s11, s11, s21
	v_cmp_gt_u32_e64 s[22:23], 5, v108
	s_nop 0
	v_readfirstlane_b32 s26, v115
	s_cmp_eq_u32 s26, 0xc0
	s_cbranch_scc1 .Lsp_wave6
	ds_read_b128 v[66:69], v112 offset:0
	ds_read_b128 v[70:73], v112 offset:32
	s_waitcnt lgkmcnt(1)
	v_mfma_f32_32x32x16_f16 v[2:17], v[74:77], v[66:69], 0
	ds_read_b128 v[66:69], v112 offset:64
	s_waitcnt lgkmcnt(1)
	v_mfma_f32_32x32x16_f16 v[2:17], v[78:81], v[70:73], v[2:17]
	ds_read_b128 v[70:73], v112 offset:96
	s_waitcnt lgkmcnt(1)
	v_mfma_f32_32x32x16_f16 v[2:17], v[82:85], v[66:69], v[2:17]
	s_waitcnt lgkmcnt(0)
	v_mfma_f32_32x32x16_f16 v[2:17], v[86:89], v[70:73], v[2:17]
	s_waitcnt lgkmcnt(0)
	ds_read_b128 v[66:69], v112 offset:4608
	ds_read_b128 v[70:73], v112 offset:4640
	s_waitcnt lgkmcnt(1)
	v_mfma_f32_32x32x16_f16 v[18:33], v[74:77], v[66:69], 0
	ds_read_b128 v[66:69], v112 offset:4672
	s_waitcnt lgkmcnt(1)
	v_mfma_f32_32x32x16_f16 v[18:33], v[78:81], v[70:73], v[18:33]
	ds_read_b128 v[70:73], v112 offset:4704
	s_waitcnt lgkmcnt(1)
	v_mfma_f32_32x32x16_f16 v[18:33], v[82:85], v[66:69], v[18:33]
	s_waitcnt lgkmcnt(0)
	v_mfma_f32_32x32x16_f16 v[18:33], v[86:89], v[70:73], v[18:33]
	v_fma_f32 v120, v2, s16, -v90
	v_exp_f32_e32 v2, v120
	v_fma_f32 v121, v3, s16, -v91
	v_exp_f32_e32 v3, v121
	v_fma_f32 v122, v4, s16, -v92
	v_exp_f32_e32 v4, v122
	v_fma_f32 v123, v5, s16, -v93
	v_exp_f32_e32 v5, v123
	v_fma_f32 v120, v6, s16, -v94
	v_exp_f32_e32 v6, v120
	v_fma_f32 v121, v7, s16, -v95
	v_exp_f32_e32 v7, v121
	v_fma_f32 v122, v8, s16, -v96
	v_exp_f32_e32 v8, v122
	v_fma_f32 v123, v9, s16, -v97
	v_exp_f32_e32 v9, v123
	v_fma_f32 v120, v10, s16, -v98
	v_exp_f32_e32 v10, v120
	v_fma_f32 v121, v11, s16, -v99
	v_exp_f32_e32 v11, v121
	v_fma_f32 v122, v12, s16, -v100
	v_exp_f32_e32 v12, v122
	v_fma_f32 v123, v13, s16, -v101
	v_exp_f32_e32 v13, v123
	v_fma_f32 v120, v14, s16, -v102
	v_exp_f32_e32 v14, v120
	v_fma_f32 v121, v15, s16, -v103
	v_exp_f32_e32 v15, v121
	v_fma_f32 v122, v16, s16, -v104
	v_exp_f32_e32 v16, v122
	v_fma_f32 v123, v17, s16, -v105
	v_exp_f32_e32 v17, v123
	global_store_dword v116, v2, s[10:11] offset:0
	global_store_dword v116, v3, s[10:11] offset:788
	global_store_dword v116, v4, s[10:11] offset:1576
	global_store_dword v116, v5, s[10:11] offset:2364
	global_store_dword v117, v6, s[10:11] offset:0
	global_store_dword v117, v7, s[10:11] offset:788
	global_store_dword v117, v8, s[10:11] offset:1576
	global_store_dword v117, v9, s[10:11] offset:2364
	global_store_dword v118, v10, s[10:11] offset:0
	global_store_dword v118, v11, s[10:11] offset:788
	global_store_dword v118, v12, s[10:11] offset:1576
	global_store_dword v118, v13, s[10:11] offset:2364
	global_store_dword v119, v14, s[10:11] offset:0
	global_store_dword v119, v15, s[10:11] offset:788
	global_store_dword v119, v16, s[10:11] offset:1576
	global_store_dword v119, v17, s[10:11] offset:2364
	ds_read_b128 v[66:69], v112 offset:9216
	ds_read_b128 v[70:73], v112 offset:9248
	s_waitcnt lgkmcnt(1)
	v_mfma_f32_32x32x16_f16 v[2:17], v[74:77], v[66:69], 0
	ds_read_b128 v[66:69], v112 offset:9280
	s_waitcnt lgkmcnt(1)
	v_mfma_f32_32x32x16_f16 v[2:17], v[78:81], v[70:73], v[2:17]
	ds_read_b128 v[70:73], v112 offset:9312
	s_waitcnt lgkmcnt(1)
	v_mfma_f32_32x32x16_f16 v[2:17], v[82:85], v[66:69], v[2:17]
	s_waitcnt lgkmcnt(0)
	v_mfma_f32_32x32x16_f16 v[2:17], v[86:89], v[70:73], v[2:17]
	v_fma_f32 v120, v18, s16, -v90
	v_exp_f32_e32 v18, v120
	v_fma_f32 v121, v19, s16, -v91
	v_exp_f32_e32 v19, v121
	v_fma_f32 v122, v20, s16, -v92
	v_exp_f32_e32 v20, v122
	v_fma_f32 v123, v21, s16, -v93
	v_exp_f32_e32 v21, v123
	v_fma_f32 v120, v22, s16, -v94
	v_exp_f32_e32 v22, v120
	v_fma_f32 v121, v23, s16, -v95
	v_exp_f32_e32 v23, v121
	v_fma_f32 v122, v24, s16, -v96
	v_exp_f32_e32 v24, v122
	v_fma_f32 v123, v25, s16, -v97
	v_exp_f32_e32 v25, v123
	v_fma_f32 v120, v26, s16, -v98
	v_exp_f32_e32 v26, v120
	v_fma_f32 v121, v27, s16, -v99
	v_exp_f32_e32 v27, v121
	v_fma_f32 v122, v28, s16, -v100
	v_exp_f32_e32 v28, v122
	v_fma_f32 v123, v29, s16, -v101
	v_exp_f32_e32 v29, v123
	v_fma_f32 v120, v30, s16, -v102
	v_exp_f32_e32 v30, v120
	v_fma_f32 v121, v31, s16, -v103
	v_exp_f32_e32 v31, v121
	v_fma_f32 v122, v32, s16, -v104
	v_exp_f32_e32 v32, v122
	v_fma_f32 v123, v33, s16, -v105
	v_exp_f32_e32 v33, v123
	global_store_dword v116, v18, s[10:11] offset:128
	global_store_dword v116, v19, s[10:11] offset:916
	global_store_dword v116, v20, s[10:11] offset:1704
	global_store_dword v116, v21, s[10:11] offset:2492
	global_store_dword v117, v22, s[10:11] offset:128
	global_store_dword v117, v23, s[10:11] offset:916
	global_store_dword v117, v24, s[10:11] offset:1704
	global_store_dword v117, v25, s[10:11] offset:2492
	global_store_dword v118, v26, s[10:11] offset:128
	global_store_dword v118, v27, s[10:11] offset:916
	global_store_dword v118, v28, s[10:11] offset:1704
	global_store_dword v118, v29, s[10:11] offset:2492
	global_store_dword v119, v30, s[10:11] offset:128
	global_store_dword v119, v31, s[10:11] offset:916
	global_store_dword v119, v32, s[10:11] offset:1704
	global_store_dword v119, v33, s[10:11] offset:2492
	ds_read_b128 v[66:69], v112 offset:13824
	ds_read_b128 v[70:73], v112 offset:13856
	s_waitcnt lgkmcnt(1)
	v_mfma_f32_32x32x16_f16 v[18:33], v[74:77], v[66:69], 0
	ds_read_b128 v[66:69], v112 offset:13888
	s_waitcnt lgkmcnt(1)
	v_mfma_f32_32x32x16_f16 v[18:33], v[78:81], v[70:73], v[18:33]
	ds_read_b128 v[70:73], v112 offset:13920
	s_waitcnt lgkmcnt(1)
	v_mfma_f32_32x32x16_f16 v[18:33], v[82:85], v[66:69], v[18:33]
	s_waitcnt lgkmcnt(0)
	v_mfma_f32_32x32x16_f16 v[18:33], v[86:89], v[70:73], v[18:33]
	v_fma_f32 v120, v2, s16, -v90
	v_exp_f32_e32 v2, v120
	v_fma_f32 v121, v3, s16, -v91
	v_exp_f32_e32 v3, v121
	v_fma_f32 v122, v4, s16, -v92
	v_exp_f32_e32 v4, v122
	v_fma_f32 v123, v5, s16, -v93
	v_exp_f32_e32 v5, v123
	v_fma_f32 v120, v6, s16, -v94
	v_exp_f32_e32 v6, v120
	v_fma_f32 v121, v7, s16, -v95
	v_exp_f32_e32 v7, v121
	v_fma_f32 v122, v8, s16, -v96
	v_exp_f32_e32 v8, v122
	v_fma_f32 v123, v9, s16, -v97
	v_exp_f32_e32 v9, v123
	v_fma_f32 v120, v10, s16, -v98
	v_exp_f32_e32 v10, v120
	v_fma_f32 v121, v11, s16, -v99
	v_exp_f32_e32 v11, v121
	v_fma_f32 v122, v12, s16, -v100
	v_exp_f32_e32 v12, v122
	v_fma_f32 v123, v13, s16, -v101
	v_exp_f32_e32 v13, v123
	v_fma_f32 v120, v14, s16, -v102
	v_exp_f32_e32 v14, v120
	v_fma_f32 v121, v15, s16, -v103
	v_exp_f32_e32 v15, v121
	v_fma_f32 v122, v16, s16, -v104
	v_exp_f32_e32 v16, v122
	v_fma_f32 v123, v17, s16, -v105
	v_exp_f32_e32 v17, v123
	global_store_dword v116, v2, s[10:11] offset:256
	global_store_dword v116, v3, s[10:11] offset:1044
	global_store_dword v116, v4, s[10:11] offset:1832
	global_store_dword v116, v5, s[10:11] offset:2620
	global_store_dword v117, v6, s[10:11] offset:256
	global_store_dword v117, v7, s[10:11] offset:1044
	global_store_dword v117, v8, s[10:11] offset:1832
	global_store_dword v117, v9, s[10:11] offset:2620
	global_store_dword v118, v10, s[10:11] offset:256
	global_store_dword v118, v11, s[10:11] offset:1044
	global_store_dword v118, v12, s[10:11] offset:1832
	global_store_dword v118, v13, s[10:11] offset:2620
	global_store_dword v119, v14, s[10:11] offset:256
	global_store_dword v119, v15, s[10:11] offset:1044
	global_store_dword v119, v16, s[10:11] offset:1832
	global_store_dword v119, v17, s[10:11] offset:2620
	ds_read_b128 v[66:69], v112 offset:18432
	ds_read_b128 v[70:73], v112 offset:18464
	s_waitcnt lgkmcnt(1)
	v_mfma_f32_32x32x16_f16 v[2:17], v[74:77], v[66:69], 0
	ds_read_b128 v[66:69], v112 offset:18496
	s_waitcnt lgkmcnt(1)
	v_mfma_f32_32x32x16_f16 v[2:17], v[78:81], v[70:73], v[2:17]
	ds_read_b128 v[70:73], v112 offset:18528
	s_waitcnt lgkmcnt(1)
	v_mfma_f32_32x32x16_f16 v[2:17], v[82:85], v[66:69], v[2:17]
	s_waitcnt lgkmcnt(0)
	v_mfma_f32_32x32x16_f16 v[2:17], v[86:89], v[70:73], v[2:17]
	v_fma_f32 v120, v18, s16, -v90
	v_exp_f32_e32 v18, v120
	v_fma_f32 v121, v19, s16, -v91
	v_exp_f32_e32 v19, v121
	v_fma_f32 v122, v20, s16, -v92
	v_exp_f32_e32 v20, v122
	v_fma_f32 v123, v21, s16, -v93
	v_exp_f32_e32 v21, v123
	v_fma_f32 v120, v22, s16, -v94
	v_exp_f32_e32 v22, v120
	v_fma_f32 v121, v23, s16, -v95
	v_exp_f32_e32 v23, v121
	v_fma_f32 v122, v24, s16, -v96
	v_exp_f32_e32 v24, v122
	v_fma_f32 v123, v25, s16, -v97
	v_exp_f32_e32 v25, v123
	v_fma_f32 v120, v26, s16, -v98
	v_exp_f32_e32 v26, v120
	v_fma_f32 v121, v27, s16, -v99
	v_exp_f32_e32 v27, v121
	v_fma_f32 v122, v28, s16, -v100
	v_exp_f32_e32 v28, v122
	v_fma_f32 v123, v29, s16, -v101
	v_exp_f32_e32 v29, v123
	v_fma_f32 v120, v30, s16, -v102
	v_exp_f32_e32 v30, v120
	v_fma_f32 v121, v31, s16, -v103
	v_exp_f32_e32 v31, v121
	v_fma_f32 v122, v32, s16, -v104
	v_exp_f32_e32 v32, v122
	v_fma_f32 v123, v33, s16, -v105
	v_exp_f32_e32 v33, v123
	global_store_dword v116, v18, s[10:11] offset:384
	global_store_dword v116, v19, s[10:11] offset:1172
	global_store_dword v116, v20, s[10:11] offset:1960
	global_store_dword v116, v21, s[10:11] offset:2748
	global_store_dword v117, v22, s[10:11] offset:384
	global_store_dword v117, v23, s[10:11] offset:1172
	global_store_dword v117, v24, s[10:11] offset:1960
	global_store_dword v117, v25, s[10:11] offset:2748
	global_store_dword v118, v26, s[10:11] offset:384
	global_store_dword v118, v27, s[10:11] offset:1172
	global_store_dword v118, v28, s[10:11] offset:1960
	global_store_dword v118, v29, s[10:11] offset:2748
	global_store_dword v119, v30, s[10:11] offset:384
	global_store_dword v119, v31, s[10:11] offset:1172
	global_store_dword v119, v32, s[10:11] offset:1960
	global_store_dword v119, v33, s[10:11] offset:2748
	ds_read_b128 v[66:69], v112 offset:23040
	ds_read_b128 v[70:73], v112 offset:23072
	s_waitcnt lgkmcnt(1)
	v_mfma_f32_32x32x16_f16 v[18:33], v[74:77], v[66:69], 0
	ds_read_b128 v[66:69], v112 offset:23104
	s_waitcnt lgkmcnt(1)
	v_mfma_f32_32x32x16_f16 v[18:33], v[78:81], v[70:73], v[18:33]
	ds_read_b128 v[70:73], v112 offset:23136
	s_waitcnt lgkmcnt(1)
	v_mfma_f32_32x32x16_f16 v[18:33], v[82:85], v[66:69], v[18:33]
	s_waitcnt lgkmcnt(0)
	v_mfma_f32_32x32x16_f16 v[18:33], v[86:89], v[70:73], v[18:33]
	v_fma_f32 v120, v2, s16, -v90
	v_exp_f32_e32 v2, v120
	v_fma_f32 v121, v3, s16, -v91
	v_exp_f32_e32 v3, v121
	v_fma_f32 v122, v4, s16, -v92
	v_exp_f32_e32 v4, v122
	v_fma_f32 v123, v5, s16, -v93
	v_exp_f32_e32 v5, v123
	v_fma_f32 v120, v6, s16, -v94
	v_exp_f32_e32 v6, v120
	v_fma_f32 v121, v7, s16, -v95
	v_exp_f32_e32 v7, v121
	v_fma_f32 v122, v8, s16, -v96
	v_exp_f32_e32 v8, v122
	v_fma_f32 v123, v9, s16, -v97
	v_exp_f32_e32 v9, v123
	v_fma_f32 v120, v10, s16, -v98
	v_exp_f32_e32 v10, v120
	v_fma_f32 v121, v11, s16, -v99
	v_exp_f32_e32 v11, v121
	v_fma_f32 v122, v12, s16, -v100
	v_exp_f32_e32 v12, v122
	v_fma_f32 v123, v13, s16, -v101
	v_exp_f32_e32 v13, v123
	v_fma_f32 v120, v14, s16, -v102
	v_exp_f32_e32 v14, v120
	v_fma_f32 v121, v15, s16, -v103
	v_exp_f32_e32 v15, v121
	v_fma_f32 v122, v16, s16, -v104
	v_exp_f32_e32 v16, v122
	v_fma_f32 v123, v17, s16, -v105
	v_exp_f32_e32 v17, v123
	global_store_dword v116, v2, s[10:11] offset:512
	global_store_dword v116, v3, s[10:11] offset:1300
	global_store_dword v116, v4, s[10:11] offset:2088
	global_store_dword v116, v5, s[10:11] offset:2876
	global_store_dword v117, v6, s[10:11] offset:512
	global_store_dword v117, v7, s[10:11] offset:1300
	global_store_dword v117, v8, s[10:11] offset:2088
	global_store_dword v117, v9, s[10:11] offset:2876
	global_store_dword v118, v10, s[10:11] offset:512
	global_store_dword v118, v11, s[10:11] offset:1300
	global_store_dword v118, v12, s[10:11] offset:2088
	global_store_dword v118, v13, s[10:11] offset:2876
	global_store_dword v119, v14, s[10:11] offset:512
	global_store_dword v119, v15, s[10:11] offset:1300
	global_store_dword v119, v16, s[10:11] offset:2088
	global_store_dword v119, v17, s[10:11] offset:2876
	ds_read_b128 v[66:69], v112 offset:27648
	ds_read_b128 v[70:73], v112 offset:27680
	s_waitcnt lgkmcnt(1)
	v_mfma_f32_32x32x16_f16 v[2:17], v[74:77], v[66:69], 0
	ds_read_b128 v[66:69], v112 offset:27712
	s_waitcnt lgkmcnt(1)
	v_mfma_f32_32x32x16_f16 v[2:17], v[78:81], v[70:73], v[2:17]
	ds_read_b128 v[70:73], v112 offset:27744
	s_waitcnt lgkmcnt(1)
	v_mfma_f32_32x32x16_f16 v[2:17], v[82:85], v[66:69], v[2:17]
	s_waitcnt lgkmcnt(0)
	v_mfma_f32_32x32x16_f16 v[2:17], v[86:89], v[70:73], v[2:17]
	v_fma_f32 v120, v18, s16, -v90
	v_exp_f32_e32 v18, v120
	v_fma_f32 v121, v19, s16, -v91
	v_exp_f32_e32 v19, v121
	v_fma_f32 v122, v20, s16, -v92
	v_exp_f32_e32 v20, v122
	v_fma_f32 v123, v21, s16, -v93
	v_exp_f32_e32 v21, v123
	v_fma_f32 v120, v22, s16, -v94
	v_exp_f32_e32 v22, v120
	v_fma_f32 v121, v23, s16, -v95
	v_exp_f32_e32 v23, v121
	v_fma_f32 v122, v24, s16, -v96
	v_exp_f32_e32 v24, v122
	v_fma_f32 v123, v25, s16, -v97
	v_exp_f32_e32 v25, v123
	v_fma_f32 v120, v26, s16, -v98
	v_exp_f32_e32 v26, v120
	v_fma_f32 v121, v27, s16, -v99
	v_exp_f32_e32 v27, v121
	v_fma_f32 v122, v28, s16, -v100
	v_exp_f32_e32 v28, v122
	v_fma_f32 v123, v29, s16, -v101
	v_exp_f32_e32 v29, v123
	v_fma_f32 v120, v30, s16, -v102
	v_exp_f32_e32 v30, v120
	v_fma_f32 v121, v31, s16, -v103
	v_exp_f32_e32 v31, v121
	v_fma_f32 v122, v32, s16, -v104
	v_exp_f32_e32 v32, v122
	v_fma_f32 v123, v33, s16, -v105
	v_exp_f32_e32 v33, v123
	global_store_dword v116, v18, s[10:11] offset:640
	global_store_dword v116, v19, s[10:11] offset:1428
	global_store_dword v116, v20, s[10:11] offset:2216
	global_store_dword v116, v21, s[10:11] offset:3004
	global_store_dword v117, v22, s[10:11] offset:640
	global_store_dword v117, v23, s[10:11] offset:1428
	global_store_dword v117, v24, s[10:11] offset:2216
	global_store_dword v117, v25, s[10:11] offset:3004
	global_store_dword v118, v26, s[10:11] offset:640
	global_store_dword v118, v27, s[10:11] offset:1428
	global_store_dword v118, v28, s[10:11] offset:2216
	global_store_dword v118, v29, s[10:11] offset:3004
	global_store_dword v119, v30, s[10:11] offset:640
	global_store_dword v119, v31, s[10:11] offset:1428
	global_store_dword v119, v32, s[10:11] offset:2216
	global_store_dword v119, v33, s[10:11] offset:3004
	s_nop 15
	s_nop 1
	v_fma_f32 v120, v2, s16, -v90
	v_exp_f32_e32 v2, v120
	v_fma_f32 v121, v3, s16, -v91
	v_exp_f32_e32 v3, v121
	v_fma_f32 v122, v4, s16, -v92
	v_exp_f32_e32 v4, v122
	v_fma_f32 v123, v5, s16, -v93
	v_exp_f32_e32 v5, v123
	v_fma_f32 v120, v6, s16, -v94
	v_exp_f32_e32 v6, v120
	v_fma_f32 v121, v7, s16, -v95
	v_exp_f32_e32 v7, v121
	v_fma_f32 v122, v8, s16, -v96
	v_exp_f32_e32 v8, v122
	v_fma_f32 v123, v9, s16, -v97
	v_exp_f32_e32 v9, v123
	v_fma_f32 v120, v10, s16, -v98
	v_exp_f32_e32 v10, v120
	v_fma_f32 v121, v11, s16, -v99
	v_exp_f32_e32 v11, v121
	v_fma_f32 v122, v12, s16, -v100
	v_exp_f32_e32 v12, v122
	v_fma_f32 v123, v13, s16, -v101
	v_exp_f32_e32 v13, v123
	v_fma_f32 v120, v14, s16, -v102
	v_exp_f32_e32 v14, v120
	v_fma_f32 v121, v15, s16, -v103
	v_exp_f32_e32 v15, v121
	v_fma_f32 v122, v16, s16, -v104
	v_exp_f32_e32 v16, v122
	v_fma_f32 v123, v17, s16, -v105
	v_exp_f32_e32 v17, v123
	s_and_b64 exec, exec, s[22:23]
	global_store_dword v116, v2, s[10:11] offset:768
	global_store_dword v116, v3, s[10:11] offset:1556
	global_store_dword v116, v4, s[10:11] offset:2344
	global_store_dword v116, v5, s[10:11] offset:3132
	global_store_dword v117, v6, s[10:11] offset:768
	global_store_dword v117, v7, s[10:11] offset:1556
	global_store_dword v117, v8, s[10:11] offset:2344
	global_store_dword v117, v9, s[10:11] offset:3132
	global_store_dword v118, v10, s[10:11] offset:768
	global_store_dword v118, v11, s[10:11] offset:1556
	global_store_dword v118, v12, s[10:11] offset:2344
	global_store_dword v118, v13, s[10:11] offset:3132
	global_store_dword v119, v14, s[10:11] offset:768
	global_store_dword v119, v15, s[10:11] offset:1556
	global_store_dword v119, v16, s[10:11] offset:2344
	global_store_dword v119, v17, s[10:11] offset:3132
	s_mov_b64 exec, s[18:19]
	s_endpgm
